# P8 epilogue: the 8 per-row step loads hoisted behind one wait; P10: one workgroup barrier per pair of expert batches (4 per token) on top of the sorted alternating sweep
# speedup vs baseline: 1.0195x; 1.0023x over previous
; __device__ __forceinline__ unsigned cvt_pk_bf16(float lo, float hi) { f32x2_t v = {lo, hi}; bf16x2_t b = __builtin_convertvector(v, bf16x2_t); return __builtin_bit_cast(unsigned, b); }
;     __device__ __forceinline__ void operator()(const pg8::f32x4 (&acc)[2][2][4][2], const pg8::Unit& u, int wr, int wc, int fr, int fq) const {
;         const int row0 = u.pm * 256 + wr * 64 + fr, col0 = u.pn * 256 + wc * 32 + 8 * fq;
;         float cw[2][8];
; #pragma unroll
;         for (int bj = 0; bj < 2; ++bj)
; #pragma unroll
;             for (int i = 0; i < 8; ++i) cw[bj][i] = cmax[col0 + bj * 128 + i] * (1.f / 127.f);
; #pragma unroll
;         for (int ai = 0; ai < 2; ++ai)
; #pragma unroll
;             for (int m = 0; m < 4; ++m) { const int row = row0 + ai * 128 + m * 16; const float ra = sa[row]; bf16_t* rowp = O + (size_t)row * ld + col0;
; #pragma unroll
;                 for (int bj = 0; bj < 2; ++bj) { float v[8];
; #pragma unroll
;                     for (int i = 0; i < 4; ++i) { const float a0 = acc[ai][bj][m][0][i], a1 = acc[ai][bj][m][1][i];
;                         v[i] = (float)__float_as_int(a0) * ra * cw[bj][i]; v[4 + i] = (float)__float_as_int(a1) * ra * cw[bj][4 + i]; }
;                     u32x4 w; w.x = cvt_pk_bf16(v[0], v[1]); w.y = cvt_pk_bf16(v[2], v[3]); w.z = cvt_pk_bf16(v[4], v[5]); w.w = cvt_pk_bf16(v[6], v[7]);
;                     *(u32x4*)(rowp + bj * 128) = w; } }
.LBB0_841:
	v_mov_b32_e32 v130, v0
	s_lshl_b32 s1, s38, 8
	v_readfirstlane_b32 s0, v130
	s_ashr_i32 s5, s0, 2
	s_andn2_b32 s5, s5, 63
	s_lshr_b32 s0, s0, 1
	s_add_i32 s5, s5, s1
	s_lshl_b32 s1, s48, 8
	s_and_b32 s0, s0, 0x60
	s_or_b32 s0, s0, s1
	v_lshrrev_b32_e32 v136, 1, v130
	v_and_or_b32 v138, v136, 24, s0
	v_readlane_b32 s0, v254, 7
	v_ashrrev_i32_e32 v139, 31, v138
	v_readlane_b32 s1, v254, 8
	v_and_or_b32 v140, v130, 15, s5
	v_ashrrev_i32_e32 v141, 31, v140
	v_lshl_add_u64 v[142:143], v[138:139], 2, s[0:1]
	v_lshl_add_u64 v[136:137], v[140:141], 2, s[14:15]
	global_load_dwordx4 v[152:155], v[142:143], off
	global_load_dword v130, v[136:137], off
	global_load_dword v210, v[136:137], off offset:64
	global_load_dword v212, v[136:137], off offset:128
	global_load_dword v214, v[136:137], off offset:192
	global_load_dword v216, v[136:137], off offset:512
	global_load_dword v218, v[136:137], off offset:576
	global_load_dword v220, v[136:137], off offset:640
	global_load_dword v222, v[136:137], off offset:704
	global_load_dwordx4 v[156:159], v[142:143], off offset:16
	global_load_dwordx4 v[160:163], v[142:143], off offset:512
	global_load_dwordx4 v[164:167], v[142:143], off offset:528
	v_cvt_f32_i32_e32 v127, v127
	v_cvt_f32_i32_e32 v126, v126
	v_cvt_f32_i32_e32 v123, v123
	v_cvt_f32_i32_e32 v122, v122
	v_cvt_f32_i32_e32 v129, v129
	v_cvt_f32_i32_e32 v128, v128
	v_cvt_f32_i32_e32 v125, v125
	v_cvt_f32_i32_e32 v124, v124
	v_cvt_f32_i32_e32 v169, v119
	v_cvt_f32_i32_e32 v168, v118
	v_cvt_f32_i32_e32 v171, v115
	v_cvt_f32_i32_e32 v170, v114
	v_cvt_f32_i32_e32 v173, v121
	v_cvt_f32_i32_e32 v172, v120
	v_cvt_f32_i32_e32 v175, v117
	v_cvt_f32_i32_e32 v174, v116
	v_lshlrev_b64 v[114:115], 12, v[140:141]
	v_lshlrev_b64 v[142:143], 1, v[138:139]
	v_lshl_add_u64 v[114:115], s[12:13], 0, v[114:115]
	v_lshl_add_u64 v[138:139], v[114:115], 0, v[142:143]
	v_or_b32_e32 v176, 16, v140
	v_ashrrev_i32_e32 v177, 31, v176
	v_lshl_add_u64 v[178:179], v[176:177], 2, s[14:15]
	v_cvt_f32_i32_e32 v111, v111
	v_cvt_f32_i32_e32 v110, v110
	v_cvt_f32_i32_e32 v107, v107
	v_cvt_f32_i32_e32 v106, v106
	v_cvt_f32_i32_e32 v113, v113
	v_cvt_f32_i32_e32 v112, v112
	v_cvt_f32_i32_e32 v109, v109
	v_cvt_f32_i32_e32 v108, v108
	v_cvt_f32_i32_e32 v103, v103
	v_cvt_f32_i32_e32 v102, v102
	v_cvt_f32_i32_e32 v99, v99
	v_cvt_f32_i32_e32 v98, v98
	v_cvt_f32_i32_e32 v105, v105
	v_cvt_f32_i32_e32 v104, v104
	v_cvt_f32_i32_e32 v101, v101
	v_cvt_f32_i32_e32 v100, v100
	v_cvt_f32_i32_e32 v95, v95
	v_cvt_f32_i32_e32 v94, v94
	v_cvt_f32_i32_e32 v91, v91
	v_cvt_f32_i32_e32 v90, v90
	v_cvt_f32_i32_e32 v97, v97
	v_cvt_f32_i32_e32 v96, v96
	v_cvt_f32_i32_e32 v93, v93
	v_cvt_f32_i32_e32 v92, v92
	v_cvt_f32_i32_e32 v87, v87
	v_cvt_f32_i32_e32 v86, v86
	v_cvt_f32_i32_e32 v83, v83
	v_cvt_f32_i32_e32 v82, v82
	v_cvt_f32_i32_e32 v89, v89
	v_cvt_f32_i32_e32 v88, v88
	v_cvt_f32_i32_e32 v85, v85
	v_cvt_f32_i32_e32 v84, v84
	v_cvt_f32_i32_e32 v79, v79
	v_cvt_f32_i32_e32 v78, v78
	v_cvt_f32_i32_e32 v75, v75
	v_cvt_f32_i32_e32 v74, v74
	v_cvt_f32_i32_e32 v81, v81
	v_cvt_f32_i32_e32 v80, v80
	v_cvt_f32_i32_e32 v77, v77
	v_cvt_f32_i32_e32 v76, v76
	v_cvt_f32_i32_e32 v71, v71
	v_cvt_f32_i32_e32 v70, v70
	v_cvt_f32_i32_e32 v67, v67
	v_cvt_f32_i32_e32 v66, v66
	v_cvt_f32_i32_e32 v73, v73
	v_cvt_f32_i32_e32 v72, v72
	v_cvt_f32_i32_e32 v69, v69
	v_cvt_f32_i32_e32 v68, v68
	v_cvt_f32_i32_e32 v63, v63
	v_cvt_f32_i32_e32 v62, v62
	v_cvt_f32_i32_e32 v59, v59
	v_cvt_f32_i32_e32 v58, v58
	s_waitcnt vmcnt(0)
	v_pk_mul_f32 v[114:115], v[152:153], s[20:21] op_sel_hi:[1,0]
	v_pk_mul_f32 v[152:153], v[130:131], v[126:127] op_sel_hi:[0,1]
	v_pk_mul_f32 v[116:117], v[156:157], s[20:21] op_sel_hi:[1,0]
	v_pk_mul_f32 v[156:157], v[130:131], v[122:123] op_sel_hi:[0,1]
	v_pk_mul_f32 v[118:119], v[154:155], s[20:21] op_sel_hi:[1,0]
	v_pk_mul_f32 v[154:155], v[130:131], v[128:129] op_sel_hi:[0,1]
	v_pk_mul_f32 v[120:121], v[158:159], s[20:21] op_sel_hi:[1,0]
	v_pk_mul_f32 v[158:159], v[130:131], v[124:125] op_sel_hi:[0,1]
	v_pk_mul_f32 v[122:123], v[160:161], s[20:21] op_sel_hi:[1,0]
	v_pk_mul_f32 v[160:161], v[130:131], v[168:169] op_sel_hi:[0,1]
	v_pk_mul_f32 v[124:125], v[164:165], s[20:21] op_sel_hi:[1,0]
	v_pk_mul_f32 v[164:165], v[130:131], v[170:171] op_sel_hi:[0,1]
	v_pk_mul_f32 v[126:127], v[162:163], s[20:21] op_sel_hi:[1,0]
	v_pk_mul_f32 v[162:163], v[130:131], v[172:173] op_sel_hi:[0,1]
	v_pk_mul_f32 v[128:129], v[166:167], s[20:21] op_sel_hi:[1,0]
	v_pk_mul_f32 v[166:167], v[130:131], v[174:175] op_sel_hi:[0,1]
	v_pk_mul_f32 v[152:153], v[114:115], v[152:153]
	v_pk_mul_f32 v[156:157], v[116:117], v[156:157]
	v_pk_mul_f32 v[154:155], v[118:119], v[154:155]
	v_pk_mul_f32 v[158:159], v[120:121], v[158:159]
	v_pk_mul_f32 v[160:161], v[122:123], v[160:161]
	v_pk_mul_f32 v[164:165], v[124:125], v[164:165]
	v_pk_mul_f32 v[162:163], v[126:127], v[162:163]
	v_pk_mul_f32 v[166:167], v[128:129], v[166:167]
	v_cvt_pk_bf16_f32 v152, v152, v153
	v_cvt_pk_bf16_f32 v153, v154, v155
	v_cvt_pk_bf16_f32 v154, v156, v157
	v_cvt_pk_bf16_f32 v155, v158, v159
	v_cvt_pk_bf16_f32 v156, v160, v161
	v_cvt_pk_bf16_f32 v157, v162, v163
	v_cvt_pk_bf16_f32 v158, v164, v165
	v_cvt_pk_bf16_f32 v159, v166, v167
	global_store_dwordx4 v[138:139], v[152:155], off
	global_store_dwordx4 v[138:139], v[156:159], off offset:256
	s_nop 0
	v_lshlrev_b64 v[154:155], 12, v[176:177]
	v_or_b32_e32 v152, 32, v140
	v_lshl_add_u64 v[154:155], s[12:13], 0, v[154:155]
	v_ashrrev_i32_e32 v153, 31, v152
	v_lshl_add_u64 v[154:155], v[154:155], 0, v[142:143]
	v_lshl_add_u64 v[156:157], v[152:153], 2, s[14:15]
	v_cvt_f32_i32_e32 v65, v65
	v_cvt_f32_i32_e32 v64, v64
; __device__ __forceinline__ unsigned cvt_pk_bf16(float lo, float hi) { f32x2_t v = {lo, hi}; bf16x2_t b = __builtin_convertvector(v, bf16x2_t); return __builtin_bit_cast(unsigned, b); }
;     __device__ __forceinline__ void operator()(const pg8::f32x4 (&acc)[2][2][4][2], const pg8::Unit& u, int wr, int wc, int fr, int fq) const {
;     ...
;             for (int m = 0; m < 4; ++m) { const int row = row0 + ai * 128 + m * 16; const float ra = sa[row]; bf16_t* rowp = O + (size_t)row * ld + col0;
; #pragma unroll
;                 for (int bj = 0; bj < 2; ++bj) { float v[8];
; #pragma unroll
;                     for (int i = 0; i < 4; ++i) { const float a0 = acc[ai][bj][m][0][i], a1 = acc[ai][bj][m][1][i];
;                         v[i] = (float)__float_as_int(a0) * ra * cw[bj][i]; v[4 + i] = (float)__float_as_int(a1) * ra * cw[bj][4 + i]; }
;                     u32x4 w; w.x = cvt_pk_bf16(v[0], v[1]); w.y = cvt_pk_bf16(v[2], v[3]); w.z = cvt_pk_bf16(v[4], v[5]); w.w = cvt_pk_bf16(v[6], v[7]);
;                     *(u32x4*)(rowp + bj * 128) = w; } }
	v_cvt_f32_i32_e32 v61, v61
	v_cvt_f32_i32_e32 v60, v60
	v_cvt_f32_i32_e32 v55, v55
	v_cvt_f32_i32_e32 v54, v54
	v_cvt_f32_i32_e32 v51, v51
	v_cvt_f32_i32_e32 v50, v50
	v_cvt_f32_i32_e32 v57, v57
	v_cvt_f32_i32_e32 v56, v56
	v_cvt_f32_i32_e32 v53, v53
	v_cvt_f32_i32_e32 v52, v52
	v_cvt_f32_i32_e32 v47, v47
	v_cvt_f32_i32_e32 v46, v46
	v_cvt_f32_i32_e32 v43, v43
	v_cvt_f32_i32_e32 v42, v42
	v_cvt_f32_i32_e32 v49, v49
	v_cvt_f32_i32_e32 v48, v48
	v_cvt_f32_i32_e32 v45, v45
	v_cvt_f32_i32_e32 v44, v44
	v_cvt_f32_i32_e32 v39, v39
	v_cvt_f32_i32_e32 v38, v38
	v_cvt_f32_i32_e32 v35, v35
	v_cvt_f32_i32_e32 v34, v34
	v_cvt_f32_i32_e32 v41, v41
	v_cvt_f32_i32_e32 v40, v40
	v_cvt_f32_i32_e32 v37, v37
	v_cvt_f32_i32_e32 v36, v36
	v_cvt_f32_i32_e32 v31, v31
	v_cvt_f32_i32_e32 v30, v30
	v_cvt_f32_i32_e32 v27, v27
	v_cvt_f32_i32_e32 v26, v26
	v_cvt_f32_i32_e32 v33, v33
	v_cvt_f32_i32_e32 v32, v32
	v_cvt_f32_i32_e32 v29, v29
	v_cvt_f32_i32_e32 v28, v28
	v_cvt_f32_i32_e32 v23, v23
	v_cvt_f32_i32_e32 v22, v22
	v_cvt_f32_i32_e32 v19, v19
	v_cvt_f32_i32_e32 v18, v18
	v_cvt_f32_i32_e32 v25, v25
	v_cvt_f32_i32_e32 v24, v24
	v_cvt_f32_i32_e32 v21, v21
	v_cvt_f32_i32_e32 v20, v20
	v_cvt_f32_i32_e32 v15, v15
	v_cvt_f32_i32_e32 v14, v14
	v_cvt_f32_i32_e32 v11, v11
	v_cvt_f32_i32_e32 v10, v10
	v_cvt_f32_i32_e32 v17, v17
	v_cvt_f32_i32_e32 v16, v16
	v_cvt_f32_i32_e32 v13, v13
	v_cvt_f32_i32_e32 v12, v12
	v_cvt_f32_i32_e32 v7, v7
	v_cvt_f32_i32_e32 v6, v6
	v_cvt_f32_i32_e32 v3, v3
	v_cvt_f32_i32_e32 v2, v2
	v_cvt_f32_i32_e32 v9, v9
	v_cvt_f32_i32_e32 v8, v8
	v_cvt_f32_i32_e32 v5, v5
	v_cvt_f32_i32_e32 v4, v4
	s_mov_b64 s[0:1], -1
	v_pk_mul_f32 v[110:111], v[210:211], v[110:111] op_sel_hi:[0,1]
	v_pk_mul_f32 v[106:107], v[210:211], v[106:107] op_sel_hi:[0,1]
	v_pk_mul_f32 v[112:113], v[210:211], v[112:113] op_sel_hi:[0,1]
	v_pk_mul_f32 v[108:109], v[210:211], v[108:109] op_sel_hi:[0,1]
	v_pk_mul_f32 v[102:103], v[210:211], v[102:103] op_sel_hi:[0,1]
	v_pk_mul_f32 v[98:99], v[210:211], v[98:99] op_sel_hi:[0,1]
	v_pk_mul_f32 v[104:105], v[210:211], v[104:105] op_sel_hi:[0,1]
	v_pk_mul_f32 v[100:101], v[210:211], v[100:101] op_sel_hi:[0,1]
	v_pk_mul_f32 v[110:111], v[114:115], v[110:111]
	v_pk_mul_f32 v[106:107], v[116:117], v[106:107]
	v_pk_mul_f32 v[112:113], v[118:119], v[112:113]
	v_pk_mul_f32 v[108:109], v[120:121], v[108:109]
	v_pk_mul_f32 v[102:103], v[122:123], v[102:103]
	v_pk_mul_f32 v[158:159], v[124:125], v[98:99]
	v_pk_mul_f32 v[104:105], v[126:127], v[104:105]
	v_pk_mul_f32 v[160:161], v[128:129], v[100:101]
	v_cvt_pk_bf16_f32 v98, v110, v111
	v_cvt_pk_bf16_f32 v99, v112, v113
	v_cvt_pk_bf16_f32 v100, v106, v107
	v_cvt_pk_bf16_f32 v101, v108, v109
	v_cvt_pk_bf16_f32 v102, v102, v103
	v_cvt_pk_bf16_f32 v103, v104, v105
	v_cvt_pk_bf16_f32 v104, v158, v159
	v_cvt_pk_bf16_f32 v105, v160, v161
	global_store_dwordx4 v[154:155], v[98:101], off
	global_store_dwordx4 v[154:155], v[102:105], off offset:256
	s_nop 0
	v_or_b32_e32 v100, 48, v140
	v_lshlrev_b64 v[102:103], 12, v[152:153]
	v_lshl_add_u64 v[102:103], s[12:13], 0, v[102:103]
	v_ashrrev_i32_e32 v101, 31, v100
	v_lshl_add_u64 v[102:103], v[102:103], 0, v[142:143]
	v_lshl_add_u64 v[104:105], v[100:101], 2, s[14:15]
	v_pk_mul_f32 v[94:95], v[212:213], v[94:95] op_sel_hi:[0,1]
	v_pk_mul_f32 v[90:91], v[212:213], v[90:91] op_sel_hi:[0,1]
	v_pk_mul_f32 v[96:97], v[212:213], v[96:97] op_sel_hi:[0,1]
	v_pk_mul_f32 v[92:93], v[212:213], v[92:93] op_sel_hi:[0,1]
	v_pk_mul_f32 v[86:87], v[212:213], v[86:87] op_sel_hi:[0,1]
	v_pk_mul_f32 v[82:83], v[212:213], v[82:83] op_sel_hi:[0,1]
	v_pk_mul_f32 v[88:89], v[212:213], v[88:89] op_sel_hi:[0,1]
	v_pk_mul_f32 v[84:85], v[212:213], v[84:85] op_sel_hi:[0,1]
	v_pk_mul_f32 v[94:95], v[114:115], v[94:95]
	v_pk_mul_f32 v[90:91], v[116:117], v[90:91]
	v_pk_mul_f32 v[96:97], v[118:119], v[96:97]
	v_pk_mul_f32 v[92:93], v[120:121], v[92:93]
	v_pk_mul_f32 v[86:87], v[122:123], v[86:87]
	v_pk_mul_f32 v[98:99], v[124:125], v[82:83]
	v_pk_mul_f32 v[88:89], v[126:127], v[88:89]
	v_pk_mul_f32 v[106:107], v[128:129], v[84:85]
	v_cvt_pk_bf16_f32 v82, v94, v95
	v_cvt_pk_bf16_f32 v83, v96, v97
	v_cvt_pk_bf16_f32 v84, v90, v91
	v_cvt_pk_bf16_f32 v85, v92, v93
	v_cvt_pk_bf16_f32 v86, v86, v87
	v_cvt_pk_bf16_f32 v87, v88, v89
	v_cvt_pk_bf16_f32 v88, v98, v99
	v_cvt_pk_bf16_f32 v89, v106, v107
	global_store_dwordx4 v[102:103], v[82:85], off
	global_store_dwordx4 v[102:103], v[86:89], off offset:256
	s_nop 0
	v_lshlrev_b64 v[84:85], 12, v[100:101]
	v_lshl_add_u64 v[84:85], s[12:13], 0, v[84:85]
	v_lshl_add_u64 v[84:85], v[84:85], 0, v[142:143]
	v_pk_mul_f32 v[78:79], v[214:215], v[78:79] op_sel_hi:[0,1]
	v_pk_mul_f32 v[74:75], v[214:215], v[74:75] op_sel_hi:[0,1]
	v_pk_mul_f32 v[80:81], v[214:215], v[80:81] op_sel_hi:[0,1]
	v_pk_mul_f32 v[76:77], v[214:215], v[76:77] op_sel_hi:[0,1]
	v_pk_mul_f32 v[70:71], v[214:215], v[70:71] op_sel_hi:[0,1]
	v_pk_mul_f32 v[66:67], v[214:215], v[66:67] op_sel_hi:[0,1]
	v_pk_mul_f32 v[72:73], v[214:215], v[72:73] op_sel_hi:[0,1]
	v_pk_mul_f32 v[68:69], v[214:215], v[68:69] op_sel_hi:[0,1]
	v_pk_mul_f32 v[78:79], v[114:115], v[78:79]
	v_pk_mul_f32 v[74:75], v[116:117], v[74:75]
	v_pk_mul_f32 v[80:81], v[118:119], v[80:81]
	v_pk_mul_f32 v[76:77], v[120:121], v[76:77]
	v_pk_mul_f32 v[70:71], v[122:123], v[70:71]
	v_pk_mul_f32 v[82:83], v[124:125], v[66:67]
	v_pk_mul_f32 v[72:73], v[126:127], v[72:73]
	v_pk_mul_f32 v[86:87], v[128:129], v[68:69]
	v_cvt_pk_bf16_f32 v66, v78, v79
	v_cvt_pk_bf16_f32 v67, v80, v81
	v_cvt_pk_bf16_f32 v68, v74, v75
	v_cvt_pk_bf16_f32 v69, v76, v77
	v_cvt_pk_bf16_f32 v70, v70, v71
	v_cvt_pk_bf16_f32 v71, v72, v73
	v_cvt_pk_bf16_f32 v72, v82, v83
; #define PG8_BAR __builtin_amdgcn_s_barrier()
; __device__ __forceinline__ unsigned cvt_pk_bf16(float lo, float hi) { f32x2_t v = {lo, hi}; bf16x2_t b = __builtin_convertvector(v, bf16x2_t); return __builtin_bit_cast(unsigned, b); }
;     ...
;         if (!has_next) break;
; #pragma unroll
;         for (int a = 0; a < 2; ++a)
; #pragma unroll
;             for (int b = 0; b < 2; ++b)
; #pragma unroll
;                 for (int m = 0; m < 4; ++m)
; #pragma unroll
;                     for (int n = 0; n < 2; ++n) acc[a][b][m][n] = (f32x4){0.f, 0.f, 0.f, 0.f};
;         cur = nxt; cA = nA; cB = nB; ++ui;
;         if constexpr (ALIGN_EPI) { if (wr == 1) PG8_BAR; }
;     }
;     __device__ __forceinline__ void operator()(const pg8::f32x4 (&acc)[2][2][4][2], const pg8::Unit& u, int wr, int wc, int fr, int fq) const {
;     ...
;             for (int m = 0; m < 4; ++m) { const int row = row0 + ai * 128 + m * 16; const float ra = sa[row]; bf16_t* rowp = O + (size_t)row * ld + col0;
; #pragma unroll
;                 for (int bj = 0; bj < 2; ++bj) { float v[8];
; #pragma unroll
;                     for (int i = 0; i < 4; ++i) { const float a0 = acc[ai][bj][m][0][i], a1 = acc[ai][bj][m][1][i];
;                         v[i] = (float)__float_as_int(a0) * ra * cw[bj][i]; v[4 + i] = (float)__float_as_int(a1) * ra * cw[bj][4 + i]; }
;                     u32x4 w; w.x = cvt_pk_bf16(v[0], v[1]); w.y = cvt_pk_bf16(v[2], v[3]); w.z = cvt_pk_bf16(v[4], v[5]); w.w = cvt_pk_bf16(v[6], v[7]);
;                     *(u32x4*)(rowp + bj * 128) = w; } }
	v_cvt_pk_bf16_f32 v73, v86, v87
	global_store_dwordx4 v[84:85], v[66:69], off
	global_store_dwordx4 v[84:85], v[70:73], off offset:256
	s_nop 0
	v_lshl_add_u64 v[68:69], v[138:139], 0, s[22:23]
	v_add_co_u32_e32 v70, vcc, s61, v138
	v_pk_mul_f32 v[62:63], v[216:217], v[62:63] op_sel_hi:[0,1]
	v_pk_mul_f32 v[58:59], v[216:217], v[58:59] op_sel_hi:[0,1]
	v_pk_mul_f32 v[64:65], v[216:217], v[64:65] op_sel_hi:[0,1]
	v_pk_mul_f32 v[60:61], v[216:217], v[60:61] op_sel_hi:[0,1]
	v_pk_mul_f32 v[54:55], v[216:217], v[54:55] op_sel_hi:[0,1]
	v_pk_mul_f32 v[50:51], v[216:217], v[50:51] op_sel_hi:[0,1]
	v_pk_mul_f32 v[56:57], v[216:217], v[56:57] op_sel_hi:[0,1]
	v_pk_mul_f32 v[52:53], v[216:217], v[52:53] op_sel_hi:[0,1]
	v_pk_mul_f32 v[62:63], v[114:115], v[62:63]
	v_pk_mul_f32 v[58:59], v[116:117], v[58:59]
	v_pk_mul_f32 v[64:65], v[118:119], v[64:65]
	v_pk_mul_f32 v[60:61], v[120:121], v[60:61]
	v_addc_co_u32_e32 v71, vcc, 0, v139, vcc
	v_pk_mul_f32 v[54:55], v[122:123], v[54:55]
	v_pk_mul_f32 v[66:67], v[124:125], v[50:51]
	v_pk_mul_f32 v[56:57], v[126:127], v[56:57]
	v_pk_mul_f32 v[72:73], v[128:129], v[52:53]
	v_cvt_pk_bf16_f32 v50, v62, v63
	v_cvt_pk_bf16_f32 v51, v64, v65
	v_cvt_pk_bf16_f32 v52, v58, v59
	v_cvt_pk_bf16_f32 v53, v60, v61
	v_cvt_pk_bf16_f32 v54, v54, v55
	v_cvt_pk_bf16_f32 v55, v56, v57
	v_cvt_pk_bf16_f32 v56, v66, v67
	v_cvt_pk_bf16_f32 v57, v72, v73
	global_store_dwordx4 v[70:71], v[50:53], off
	global_store_dwordx4 v[68:69], v[54:57], off offset:256
	s_nop 0
	v_lshl_add_u64 v[52:53], v[138:139], 0, s[24:25]
	v_add_co_u32_e32 v54, vcc, s62, v138
	v_pk_mul_f32 v[46:47], v[218:219], v[46:47] op_sel_hi:[0,1]
	v_pk_mul_f32 v[42:43], v[218:219], v[42:43] op_sel_hi:[0,1]
	v_pk_mul_f32 v[48:49], v[218:219], v[48:49] op_sel_hi:[0,1]
	v_pk_mul_f32 v[44:45], v[218:219], v[44:45] op_sel_hi:[0,1]
	v_pk_mul_f32 v[38:39], v[218:219], v[38:39] op_sel_hi:[0,1]
	v_pk_mul_f32 v[34:35], v[218:219], v[34:35] op_sel_hi:[0,1]
	v_pk_mul_f32 v[40:41], v[218:219], v[40:41] op_sel_hi:[0,1]
	v_pk_mul_f32 v[36:37], v[218:219], v[36:37] op_sel_hi:[0,1]
	v_pk_mul_f32 v[46:47], v[114:115], v[46:47]
	v_pk_mul_f32 v[42:43], v[116:117], v[42:43]
	v_pk_mul_f32 v[48:49], v[118:119], v[48:49]
	v_pk_mul_f32 v[44:45], v[120:121], v[44:45]
	v_addc_co_u32_e32 v55, vcc, 0, v139, vcc
	v_pk_mul_f32 v[38:39], v[122:123], v[38:39]
	v_pk_mul_f32 v[50:51], v[124:125], v[34:35]
	v_pk_mul_f32 v[40:41], v[126:127], v[40:41]
	v_pk_mul_f32 v[56:57], v[128:129], v[36:37]
	v_cvt_pk_bf16_f32 v34, v46, v47
	v_cvt_pk_bf16_f32 v35, v48, v49
	v_cvt_pk_bf16_f32 v36, v42, v43
	v_cvt_pk_bf16_f32 v37, v44, v45
	v_cvt_pk_bf16_f32 v38, v38, v39
	v_cvt_pk_bf16_f32 v39, v40, v41
	v_cvt_pk_bf16_f32 v40, v50, v51
	v_cvt_pk_bf16_f32 v41, v56, v57
	global_store_dwordx4 v[54:55], v[34:37], off
	global_store_dwordx4 v[52:53], v[38:41], off offset:256
	s_nop 0
	v_lshl_add_u64 v[36:37], v[138:139], 0, s[26:27]
	v_add_co_u32_e32 v38, vcc, s63, v138
	v_pk_mul_f32 v[30:31], v[220:221], v[30:31] op_sel_hi:[0,1]
	v_pk_mul_f32 v[26:27], v[220:221], v[26:27] op_sel_hi:[0,1]
	v_pk_mul_f32 v[32:33], v[220:221], v[32:33] op_sel_hi:[0,1]
	v_pk_mul_f32 v[28:29], v[220:221], v[28:29] op_sel_hi:[0,1]
	v_pk_mul_f32 v[22:23], v[220:221], v[22:23] op_sel_hi:[0,1]
	v_pk_mul_f32 v[18:19], v[220:221], v[18:19] op_sel_hi:[0,1]
	v_pk_mul_f32 v[24:25], v[220:221], v[24:25] op_sel_hi:[0,1]
	v_pk_mul_f32 v[20:21], v[220:221], v[20:21] op_sel_hi:[0,1]
	v_pk_mul_f32 v[30:31], v[114:115], v[30:31]
	v_pk_mul_f32 v[26:27], v[116:117], v[26:27]
	v_pk_mul_f32 v[32:33], v[118:119], v[32:33]
	v_pk_mul_f32 v[28:29], v[120:121], v[28:29]
	v_addc_co_u32_e32 v39, vcc, 0, v139, vcc
	v_pk_mul_f32 v[22:23], v[122:123], v[22:23]
	v_pk_mul_f32 v[34:35], v[124:125], v[18:19]
	v_pk_mul_f32 v[24:25], v[126:127], v[24:25]
	v_pk_mul_f32 v[40:41], v[128:129], v[20:21]
	v_cvt_pk_bf16_f32 v18, v30, v31
	v_cvt_pk_bf16_f32 v19, v32, v33
	v_cvt_pk_bf16_f32 v20, v26, v27
	v_cvt_pk_bf16_f32 v21, v28, v29
	v_cvt_pk_bf16_f32 v22, v22, v23
	v_cvt_pk_bf16_f32 v23, v24, v25
	v_cvt_pk_bf16_f32 v24, v34, v35
	v_cvt_pk_bf16_f32 v25, v40, v41
	global_store_dwordx4 v[38:39], v[18:21], off
	global_store_dwordx4 v[36:37], v[22:25], off offset:256
	s_nop 0
	s_andn2_b64 vcc, exec, s[6:7]
	v_add_co_u32_e64 v22, s[6:7], s64, v138
	v_lshl_add_u64 v[20:21], v[138:139], 0, s[28:29]
	s_nop 0
	v_addc_co_u32_e64 v23, s[6:7], 0, v139, s[6:7]
	v_pk_mul_f32 v[14:15], v[222:223], v[14:15] op_sel_hi:[0,1]
	v_pk_mul_f32 v[10:11], v[222:223], v[10:11] op_sel_hi:[0,1]
	v_pk_mul_f32 v[16:17], v[222:223], v[16:17] op_sel_hi:[0,1]
	v_pk_mul_f32 v[12:13], v[222:223], v[12:13] op_sel_hi:[0,1]
	v_pk_mul_f32 v[6:7], v[222:223], v[6:7] op_sel_hi:[0,1]
	v_pk_mul_f32 v[2:3], v[222:223], v[2:3] op_sel_hi:[0,1]
	v_pk_mul_f32 v[8:9], v[222:223], v[8:9] op_sel_hi:[0,1]
	v_pk_mul_f32 v[4:5], v[222:223], v[4:5] op_sel_hi:[0,1]
	v_pk_mul_f32 v[14:15], v[114:115], v[14:15]
	v_pk_mul_f32 v[10:11], v[116:117], v[10:11]
	v_pk_mul_f32 v[16:17], v[118:119], v[16:17]
	v_pk_mul_f32 v[12:13], v[120:121], v[12:13]
	v_pk_mul_f32 v[6:7], v[122:123], v[6:7]
	v_pk_mul_f32 v[18:19], v[124:125], v[2:3]
	v_pk_mul_f32 v[8:9], v[126:127], v[8:9]
	v_pk_mul_f32 v[24:25], v[128:129], v[4:5]
	v_cvt_pk_bf16_f32 v2, v14, v15
	v_cvt_pk_bf16_f32 v3, v16, v17
	v_cvt_pk_bf16_f32 v4, v10, v11
	v_cvt_pk_bf16_f32 v5, v12, v13
	v_cvt_pk_bf16_f32 v6, v6, v7
	v_cvt_pk_bf16_f32 v7, v8, v9
	v_cvt_pk_bf16_f32 v8, v18, v19
	v_cvt_pk_bf16_f32 v9, v24, v25
	global_store_dwordx4 v[22:23], v[2:5], off
	global_store_dwordx4 v[20:21], v[6:9], off offset:256
	s_cbranch_vccnz .LBB0_830
	s_andn2_b64 vcc, exec, s[10:11]
	s_cbranch_vccnz .LBB0_829
	s_barrier
	s_branch .LBB0_829

.LBB0_1019:
	s_barrier
	v_mov_b32_e32 v88, 0
	v_dot8c_i32_i4_e32 v88, v248, v70
	v_dot8c_i32_i4_e32 v88, v250, v71
	v_mov_b32_e32 v74, 0
	v_mov_b32_e32 v75, 0
	v_mov_b32_e32 v76, 0
	v_lshlrev_b32_e32 v88, 4, v88
	v_mov_b32_e32 v77, 0
	v_mov_b32_e32 v78, 0
	v_mov_b32_e32 v79, 0
	v_mov_b32_e32 v80, 0
	v_mov_b32_e32 v81, 0
	v_mov_b32_e32 v82, 0
	v_mov_b32_e32 v83, 0
	v_mov_b32_e32 v84, 0
	v_mov_b32_e32 v85, 0
	v_mov_b32_e32 v86, 0
	v_mov_b32_e32 v87, 0
	v_dot8c_i32_i4_e32 v88, v247, v70
	v_mov_b32_e32 v70, 0
	v_dot8c_i32_i4_e32 v74, v248, v188
	v_dot8c_i32_i4_e32 v75, v248, v184
	v_dot8c_i32_i4_e32 v76, v248, v180
	v_dot8c_i32_i4_e32 v77, v248, v176
	v_dot8c_i32_i4_e32 v78, v248, v172
	v_dot8c_i32_i4_e32 v79, v248, v168
	v_dot8c_i32_i4_e32 v80, v248, v164
	v_dot8c_i32_i4_e32 v81, v248, v160
	v_dot8c_i32_i4_e32 v82, v248, v156
	v_dot8c_i32_i4_e32 v83, v248, v152
	v_dot8c_i32_i4_e32 v84, v248, v148
	v_dot8c_i32_i4_e32 v85, v248, v144
	v_dot8c_i32_i4_e32 v86, v248, v116
	v_dot8c_i32_i4_e32 v87, v248, v112
	v_dot8c_i32_i4_e32 v70, v248, v66
	v_dot8c_i32_i4_e32 v74, v250, v189
	v_dot8c_i32_i4_e32 v75, v250, v185
	v_dot8c_i32_i4_e32 v76, v250, v181
	v_dot8c_i32_i4_e32 v77, v250, v177
	v_dot8c_i32_i4_e32 v78, v250, v173
	v_dot8c_i32_i4_e32 v79, v250, v169
	v_dot8c_i32_i4_e32 v80, v250, v165
	v_dot8c_i32_i4_e32 v81, v250, v161
	v_dot8c_i32_i4_e32 v82, v250, v157
	v_dot8c_i32_i4_e32 v83, v250, v153
	v_dot8c_i32_i4_e32 v84, v250, v149
	v_dot8c_i32_i4_e32 v85, v250, v145
	v_dot8c_i32_i4_e32 v86, v250, v117
	v_dot8c_i32_i4_e32 v87, v250, v113
	v_dot8c_i32_i4_e32 v70, v250, v67
	v_lshlrev_b32_e32 v74, 4, v74
	v_lshlrev_b32_e32 v75, 4, v75
	v_lshlrev_b32_e32 v76, 4, v76
	v_lshlrev_b32_e32 v77, 4, v77
	v_lshlrev_b32_e32 v78, 4, v78
	v_lshlrev_b32_e32 v79, 4, v79
	v_lshlrev_b32_e32 v80, 4, v80
	v_lshlrev_b32_e32 v81, 4, v81
	v_lshlrev_b32_e32 v82, 4, v82
	v_lshlrev_b32_e32 v83, 4, v83
	v_lshlrev_b32_e32 v84, 4, v84
	v_lshlrev_b32_e32 v85, 4, v85
	v_lshlrev_b32_e32 v86, 4, v86
	v_lshlrev_b32_e32 v87, 4, v87
	v_lshlrev_b32_e32 v70, 4, v70
	v_dot8c_i32_i4_e32 v74, v247, v188
	v_dot8c_i32_i4_e32 v75, v247, v184
	v_dot8c_i32_i4_e32 v76, v247, v180
	v_dot8c_i32_i4_e32 v77, v247, v176
	v_dot8c_i32_i4_e32 v78, v247, v172
	v_dot8c_i32_i4_e32 v79, v247, v168
	v_dot8c_i32_i4_e32 v80, v247, v164
	v_dot8c_i32_i4_e32 v81, v247, v160
	v_dot8c_i32_i4_e32 v82, v247, v156
	v_dot8c_i32_i4_e32 v83, v247, v152
	v_dot8c_i32_i4_e32 v84, v247, v148
	v_dot8c_i32_i4_e32 v85, v247, v144
	v_dot8c_i32_i4_e32 v86, v247, v116
	v_dot8c_i32_i4_e32 v87, v247, v112
	v_dot8c_i32_i4_e32 v70, v247, v66
	v_dot8c_i32_i4_e32 v74, v249, v189
	v_dot8c_i32_i4_e32 v75, v249, v185
	v_dot8c_i32_i4_e32 v76, v249, v181
	v_dot8c_i32_i4_e32 v77, v249, v177
	v_dot8c_i32_i4_e32 v78, v249, v173
	v_dot8c_i32_i4_e32 v79, v249, v169
	v_dot8c_i32_i4_e32 v80, v249, v165
	v_dot8c_i32_i4_e32 v81, v249, v161
	v_dot8c_i32_i4_e32 v82, v249, v157
	v_dot8c_i32_i4_e32 v83, v249, v153
	v_dot8c_i32_i4_e32 v84, v249, v149
	v_dot8c_i32_i4_e32 v85, v249, v145
	v_dot8c_i32_i4_e32 v86, v249, v117
	v_dot8c_i32_i4_e32 v87, v249, v113
	v_dot8c_i32_i4_e32 v88, v249, v71
	v_dot8c_i32_i4_e32 v70, v249, v67
	v_permlane32_swap_b32_e32 v74, v82
	v_permlane32_swap_b32_e32 v75, v83
	v_permlane32_swap_b32_e32 v76, v84
	v_permlane32_swap_b32_e32 v77, v85
	v_permlane32_swap_b32_e32 v78, v86
	v_permlane32_swap_b32_e32 v79, v87
	v_permlane32_swap_b32_e32 v80, v88
	v_permlane32_swap_b32_e32 v81, v70
	v_add_u32_e32 v66, v74, v82
	v_add_u32_e32 v67, v75, v83
	v_add_u32_e32 v71, v76, v84
	v_add_u32_e32 v74, v77, v85
	v_add_u32_e32 v75, v78, v86
	v_add_u32_e32 v76, v79, v87
	v_add_u32_e32 v77, v80, v88
	v_add_u32_e32 v70, v81, v70
	v_permlane16_swap_b32_e32 v66, v75
	v_permlane16_swap_b32_e32 v67, v76
	v_permlane16_swap_b32_e32 v71, v77
	v_permlane16_swap_b32_e32 v74, v70
	v_add_u32_e32 v66, v66, v75
	v_add_u32_e32 v67, v67, v76
	v_add_u32_e32 v71, v71, v77
	v_add_u32_e32 v70, v74, v70
	v_cndmask_b32_e64 v74, v71, v66, s[0:1]
	v_cndmask_b32_e64 v66, v66, v71, s[0:1]
	v_cndmask_b32_e64 v71, v70, v67, s[0:1]
	v_cndmask_b32_e64 v67, v67, v70, s[0:1]
	v_add_u32_dpp v66, v66, v74 quad_perm:[2,3,0,1] row_mask:0xf bank_mask:0xf bound_ctrl:1
	s_sub_i32 s4, s21, 32
	v_add_u32_dpp v67, v67, v71 quad_perm:[2,3,0,1] row_mask:0xf bank_mask:0xf bound_ctrl:1
	v_cndmask_b32_e64 v70, v67, v66, s[2:3]
	v_cndmask_b32_e64 v66, v66, v67, s[2:3]
	s_cmp_lt_u32 s25, 4
	s_cselect_b64 vcc, -1, 0
	v_add_u32_dpp v66, v66, v70 quad_perm:[1,0,3,2] row_mask:0xf bank_mask:0xf bound_ctrl:1
	v_cndmask_b32_e32 v70, v234, v233, vcc
	v_cndmask_b32_e32 v71, v230, v229, vcc
	v_add_u32_dpp v66, v66, v66 row_ror:8 row_mask:0xf bank_mask:0xf bound_ctrl:1
	s_cmp_eq_u32 s21, 32
	s_nop 0
	v_add_u32_dpp v67, v66, v66 row_ror:4 row_mask:0xf bank_mask:0xf bound_ctrl:1
	v_and_or_b32 v66, s4, 32, v193
	v_lshlrev_b32_e32 v66, 2, v66
	v_cvt_f32_i32_e32 v74, v67
	ds_bpermute_b32 v75, v66, v70
	v_and_b32_e32 v67, 0xffff0000, v71
	ds_bpermute_b32 v76, v66, v67
	v_add_f32_e32 v71, v251, v74
	v_mul_f32_e32 v71, v244, v71
	s_waitcnt lgkmcnt(1)
	v_mul_f32_e32 v74, v71, v75
	v_fma_f32 v71, |v74|, s28, 1.0
	v_rcp_f32_e32 v75, v71
	v_mul_f32_e32 v79, v74, v74
	v_mul_f32_e32 v79, 0xbf38aa3b, v79
	v_exp_f32_e32 v79, v79
	v_fmamk_f32 v78, v75, 0x3f07dc22, v227
	v_fmaak_f32 v78, v75, v78, 0x3f35f0e3
	v_fmaak_f32 v78, v75, v78, 0xbe11a98e
	v_cndmask_b32_e32 v71, v236, v235, vcc
	v_fmaak_f32 v78, v75, v78, 0x3e027906
	ds_bpermute_b32 v77, v66, v71
	v_mul_f32_e32 v75, v75, v78
	v_mul_f32_e32 v75, v79, v75
	v_mul_f32_e32 v78, v74, v75
	v_fma_f32 v75, -v74, v75, v74
	v_cmp_gt_f32_e32 vcc, 0, v74
	s_nop 1
	v_cndmask_b32_e32 v74, v75, v78, vcc
	s_waitcnt lgkmcnt(1)
	v_mul_f32_e32 v74, v74, v76
	s_cselect_b64 vcc, -1, 0
	s_cmp_gt_u32 s25, 5
	s_waitcnt lgkmcnt(0)
	v_mul_f32_e32 v74, v74, v77
	s_cselect_b64 s[22:23], -1, 0
	s_cmp_lt_u32 s25, 6
	v_fma_mixlo_f16 v116, v74, s16, 0
	s_cselect_b64 s[4:5], -1, 0
	v_and_b32_e32 v117, 0xffff, v116
	v_cndmask_b32_e64 v74, v242, v232, s[4:5]
	s_add_i32 s24, s21, 1
	s_add_i32 s35, s21, 2
	s_add_i32 s36, s21, 3
	s_add_i32 s37, s21, 4
	s_add_i32 s38, s21, 5
	s_add_i32 s39, s21, 6
	s_add_i32 s40, s21, 7
	s_add_i32 s49, s21, 8
	s_add_i32 s50, s21, 9
	s_add_i32 s51, s21, 10
	s_add_i32 s52, s21, 11
	s_add_i32 s53, s21, 12
	s_add_i32 s54, s21, 13
	s_add_i32 s55, s21, 14
	s_add_i32 s56, s21, 15
	v_cndmask_b32_e32 v136, v74, v231, vcc
	v_readlane_b32 s47, v117, 0
	v_readlane_b32 s48, v117, 1
	s_cmp_lg_u32 s21, 32
	v_readlane_b32 s4, v136, s21
	s_nop 1
	v_lshl_or_b32 v74, s4, 10, v194
	v_readlane_b32 s4, v136, s24
	s_nop 1
	v_lshl_or_b32 v75, s4, 10, v194
	global_load_dwordx4 v[78:81], v74, s[10:11]
	s_nop 0
	global_load_dwordx4 v[74:77], v75, s[10:11]
	v_readlane_b32 s45, v117, 2
	v_readlane_b32 s46, v117, 3
	v_readlane_b32 s4, v136, s35
	s_nop 1
	v_lshl_or_b32 v82, s4, 10, v194
	v_readlane_b32 s4, v136, s36
	s_nop 1
	v_lshl_or_b32 v83, s4, 10, v194
	global_load_dwordx4 v[86:89], v82, s[10:11]
	s_nop 0
	global_load_dwordx4 v[82:85], v83, s[10:11]
	v_readlane_b32 s43, v117, 16
	v_readlane_b32 s44, v117, 17
	v_readlane_b32 s4, v136, s37
	s_nop 1
	v_lshl_or_b32 v90, s4, 10, v194
	v_readlane_b32 s4, v136, s38
	s_nop 1
	v_lshl_or_b32 v91, s4, 10, v194
	global_load_dwordx4 v[94:97], v90, s[10:11]
	s_nop 0
	global_load_dwordx4 v[90:93], v91, s[10:11]
	v_readlane_b32 s41, v117, 18
	v_readlane_b32 s42, v117, 19
	v_readlane_b32 s4, v136, s39
	s_nop 1
	v_lshl_or_b32 v98, s4, 10, v194
	v_readlane_b32 s4, v136, s40
	s_nop 1
	v_lshl_or_b32 v99, s4, 10, v194
	global_load_dwordx4 v[102:105], v98, s[10:11]
	s_nop 0
	global_load_dwordx4 v[98:101], v99, s[10:11]
	v_readlane_b32 s39, v117, 32
	v_readlane_b32 s40, v117, 33
	v_readlane_b32 s4, v136, s49
	s_nop 1
	v_lshl_or_b32 v106, s4, 10, v194
	v_readlane_b32 s4, v136, s50
	s_nop 1
	v_lshl_or_b32 v107, s4, 10, v194
	global_load_dwordx4 v[110:113], v106, s[10:11]
	s_nop 0
	global_load_dwordx4 v[106:109], v107, s[10:11]
	v_readlane_b32 s37, v117, 34
	v_readlane_b32 s38, v117, 35
	v_readlane_b32 s4, v136, s51
	s_nop 1
	v_lshl_or_b32 v120, s4, 10, v194
	v_readlane_b32 s4, v136, s52
	s_nop 1
	v_lshl_or_b32 v121, s4, 10, v194
	global_load_dwordx4 v[124:127], v120, s[10:11]
	s_nop 0
	global_load_dwordx4 v[120:123], v121, s[10:11]
	v_readlane_b32 s35, v117, 48
	v_readlane_b32 s36, v117, 49
	v_readlane_b32 s4, v136, s53
	s_nop 1
	v_lshl_or_b32 v128, s4, 10, v194
	v_readlane_b32 s4, v136, s54
	s_nop 1
	v_lshl_or_b32 v129, s4, 10, v194
	global_load_dwordx4 v[132:135], v128, s[10:11]
	s_nop 0
	global_load_dwordx4 v[128:131], v129, s[10:11]
	v_readlane_b32 s4, v117, 50
	v_readlane_b32 s5, v117, 51
	v_readlane_b32 s24, v136, s55
	s_nop 1
	v_lshl_or_b32 v117, s24, 10, v194
	v_readlane_b32 s24, v136, s56
	s_nop 1
	v_lshl_or_b32 v136, s24, 10, v194
	global_load_dwordx4 v[140:143], v117, s[10:11]
	s_nop 0
	global_load_dwordx4 v[136:139], v136, s[10:11]
	s_cbranch_scc1 .LBB0_1021
	s_waitcnt vmcnt(16)
	s_bfe_i32 s60, s34, 0x10000
	v_alignbit_b32 v237, v237, v237, 16
	v_alignbit_b32 v238, v238, v238, 16
	v_xor_b32_e32 v237, s60, v237
	v_xor_b32_e32 v238, s60, v238
	s_nop 1
	s_mov_b32 s58, 0x99999999
	s_mov_b32 s59, 0x99999999
	v_min_u32_dpp v202, v237, v237 quad_perm:[1,0,3,2] row_mask:0xf bank_mask:0xf
	v_max_u32_dpp v203, v237, v237 quad_perm:[1,0,3,2] row_mask:0xf bank_mask:0xf
	v_min_u32_dpp v204, v238, v238 quad_perm:[1,0,3,2] row_mask:0xf bank_mask:0xf
	v_max_u32_dpp v205, v238, v238 quad_perm:[1,0,3,2] row_mask:0xf bank_mask:0xf
	v_cndmask_b32_e64 v237, v203, v202, s[58:59]
	v_cndmask_b32_e64 v238, v205, v204, s[58:59]
	s_mov_b32 s58, 0xcc33cc33
	s_mov_b32 s59, 0xcc33cc33
	v_min_u32_dpp v202, v237, v237 quad_perm:[2,3,0,1] row_mask:0xf bank_mask:0xf
	v_max_u32_dpp v203, v237, v237 quad_perm:[2,3,0,1] row_mask:0xf bank_mask:0xf
	v_min_u32_dpp v204, v238, v238 quad_perm:[2,3,0,1] row_mask:0xf bank_mask:0xf
	v_max_u32_dpp v205, v238, v238 quad_perm:[2,3,0,1] row_mask:0xf bank_mask:0xf
	v_cndmask_b32_e64 v237, v203, v202, s[58:59]
	v_cndmask_b32_e64 v238, v205, v204, s[58:59]
	s_mov_b32 s58, 0xaa55aa55
	s_mov_b32 s59, 0xaa55aa55
	v_min_u32_dpp v202, v237, v237 quad_perm:[1,0,3,2] row_mask:0xf bank_mask:0xf
	v_max_u32_dpp v203, v237, v237 quad_perm:[1,0,3,2] row_mask:0xf bank_mask:0xf
	v_min_u32_dpp v204, v238, v238 quad_perm:[1,0,3,2] row_mask:0xf bank_mask:0xf
	v_max_u32_dpp v205, v238, v238 quad_perm:[1,0,3,2] row_mask:0xf bank_mask:0xf
	v_cndmask_b32_e64 v237, v203, v202, s[58:59]
	v_cndmask_b32_e64 v238, v205, v204, s[58:59]
	s_mov_b32 s58, 0xf00ff00f
	s_mov_b32 s59, 0xf00ff00f
	v_min_u32_dpp v202, v237, v237 row_ror:8 row_mask:0xf bank_mask:0xf
	v_max_u32_dpp v203, v237, v237 row_ror:8 row_mask:0xf bank_mask:0xf
	v_min_u32_dpp v204, v238, v238 row_ror:8 row_mask:0xf bank_mask:0xf
	v_max_u32_dpp v205, v238, v238 row_ror:8 row_mask:0xf bank_mask:0xf
	v_cndmask_b32_e64 v237, v203, v202, s[58:59]
	v_cndmask_b32_e64 v238, v205, v204, s[58:59]
	s_mov_b32 s58, 0xc3c3c3c3
	s_mov_b32 s59, 0xc3c3c3c3
	v_min_u32_dpp v202, v237, v237 quad_perm:[2,3,0,1] row_mask:0xf bank_mask:0xf
	v_max_u32_dpp v203, v237, v237 quad_perm:[2,3,0,1] row_mask:0xf bank_mask:0xf
	v_min_u32_dpp v204, v238, v238 quad_perm:[2,3,0,1] row_mask:0xf bank_mask:0xf
	v_max_u32_dpp v205, v238, v238 quad_perm:[2,3,0,1] row_mask:0xf bank_mask:0xf
	v_cndmask_b32_e64 v237, v203, v202, s[58:59]
; __device__ __forceinline__ void expert_tokens(const unsigned char* __restrict__ UV, const float* __restrict__ US, const float* __restrict__ VS, ...
;     ...
;         const unsigned nw0 = (unsigned)IDX[(size_t)tn * 128 + lane], nw1 = (unsigned)IDX[(size_t)tn * 128 + 64 + lane];
;         const int ni0 = (int)nw0 & rmask, ni1 = (int)nw1 & rmask;
	v_cndmask_b32_e64 v238, v205, v204, s[58:59]
	s_mov_b32 s58, 0xa5a5a5a5
	s_mov_b32 s59, 0xa5a5a5a5
	v_min_u32_dpp v202, v237, v237 quad_perm:[1,0,3,2] row_mask:0xf bank_mask:0xf
	v_max_u32_dpp v203, v237, v237 quad_perm:[1,0,3,2] row_mask:0xf bank_mask:0xf
	v_min_u32_dpp v204, v238, v238 quad_perm:[1,0,3,2] row_mask:0xf bank_mask:0xf
	v_max_u32_dpp v205, v238, v238 quad_perm:[1,0,3,2] row_mask:0xf bank_mask:0xf
	v_cndmask_b32_e64 v237, v203, v202, s[58:59]
	v_cndmask_b32_e64 v238, v205, v204, s[58:59]
	s_mov_b32 s58, 0xf0f00f0f
	s_mov_b32 s59, 0xf0f00f0f
	v_mov_b32_dpp v202, v237 row_half_mirror row_mask:0xf bank_mask:0xf
	v_mov_b32_dpp v204, v238 row_half_mirror row_mask:0xf bank_mask:0xf
	s_nop 0
	v_max_u32_dpp v203, v202, v237 quad_perm:[3,2,1,0] row_mask:0xf bank_mask:0xf
	v_max_u32_dpp v205, v204, v238 quad_perm:[3,2,1,0] row_mask:0xf bank_mask:0xf
	v_min_u32_dpp v202, v202, v237 quad_perm:[3,2,1,0] row_mask:0xf bank_mask:0xf
	v_min_u32_dpp v204, v204, v238 quad_perm:[3,2,1,0] row_mask:0xf bank_mask:0xf
	v_cndmask_b32_e64 v237, v203, v202, s[58:59]
	v_cndmask_b32_e64 v238, v205, v204, s[58:59]
	s_mov_b32 s58, 0xff0000ff
	s_mov_b32 s59, 0xff0000ff
	v_min_u32_dpp v202, v237, v237 row_ror:8 row_mask:0xf bank_mask:0xf
	v_max_u32_dpp v203, v237, v237 row_ror:8 row_mask:0xf bank_mask:0xf
	v_min_u32_dpp v204, v238, v238 row_ror:8 row_mask:0xf bank_mask:0xf
	v_max_u32_dpp v205, v238, v238 row_ror:8 row_mask:0xf bank_mask:0xf
	v_cndmask_b32_e64 v237, v203, v202, s[58:59]
	v_cndmask_b32_e64 v238, v205, v204, s[58:59]
	s_mov_b32 s58, 0xcccc3333
	s_mov_b32 s59, 0xcccc3333
	v_min_u32_dpp v202, v237, v237 quad_perm:[2,3,0,1] row_mask:0xf bank_mask:0xf
	v_max_u32_dpp v203, v237, v237 quad_perm:[2,3,0,1] row_mask:0xf bank_mask:0xf
	v_min_u32_dpp v204, v238, v238 quad_perm:[2,3,0,1] row_mask:0xf bank_mask:0xf
	v_max_u32_dpp v205, v238, v238 quad_perm:[2,3,0,1] row_mask:0xf bank_mask:0xf
	v_cndmask_b32_e64 v237, v203, v202, s[58:59]
	v_cndmask_b32_e64 v238, v205, v204, s[58:59]
	s_mov_b32 s58, 0xaaaa5555
	s_mov_b32 s59, 0xaaaa5555
	v_min_u32_dpp v202, v237, v237 quad_perm:[1,0,3,2] row_mask:0xf bank_mask:0xf
	v_max_u32_dpp v203, v237, v237 quad_perm:[1,0,3,2] row_mask:0xf bank_mask:0xf
	v_min_u32_dpp v204, v238, v238 quad_perm:[1,0,3,2] row_mask:0xf bank_mask:0xf
	v_max_u32_dpp v205, v238, v238 quad_perm:[1,0,3,2] row_mask:0xf bank_mask:0xf
	v_cndmask_b32_e64 v237, v203, v202, s[58:59]
	v_cndmask_b32_e64 v238, v205, v204, s[58:59]
	s_nop 1
	v_permlane16_swap_b32_e32 v237, v238
	s_mov_b32 s58, -1
	s_mov_b32 s59, 0
	v_min_u32_e32 v202, v237, v238
	v_max_u32_e32 v203, v237, v238
	v_cndmask_b32_e64 v237, v203, v202, s[58:59]
	v_cndmask_b32_e64 v238, v202, v203, s[58:59]
	s_mov_b32 s58, 0xf0f0f0f
	s_mov_b32 s59, 0xf0f0f0f0
	v_mov_b32_dpp v202, v237 row_half_mirror row_mask:0xf bank_mask:0xf
	v_mov_b32_dpp v204, v238 row_half_mirror row_mask:0xf bank_mask:0xf
	s_nop 0
	v_max_u32_dpp v203, v202, v237 quad_perm:[3,2,1,0] row_mask:0xf bank_mask:0xf
	v_max_u32_dpp v205, v204, v238 quad_perm:[3,2,1,0] row_mask:0xf bank_mask:0xf
	v_min_u32_dpp v202, v202, v237 quad_perm:[3,2,1,0] row_mask:0xf bank_mask:0xf
	v_min_u32_dpp v204, v204, v238 quad_perm:[3,2,1,0] row_mask:0xf bank_mask:0xf
	v_cndmask_b32_e64 v237, v203, v202, s[58:59]
	v_cndmask_b32_e64 v238, v205, v204, s[58:59]
	s_mov_b32 s58, 0xff00ff
	s_mov_b32 s59, 0xff00ff00
	v_min_u32_dpp v202, v237, v237 row_ror:8 row_mask:0xf bank_mask:0xf
	v_max_u32_dpp v203, v237, v237 row_ror:8 row_mask:0xf bank_mask:0xf
	v_min_u32_dpp v204, v238, v238 row_ror:8 row_mask:0xf bank_mask:0xf
	v_max_u32_dpp v205, v238, v238 row_ror:8 row_mask:0xf bank_mask:0xf
	v_cndmask_b32_e64 v237, v203, v202, s[58:59]
	v_cndmask_b32_e64 v238, v205, v204, s[58:59]
	s_mov_b32 s58, 0x33333333
	s_mov_b32 s59, 0xcccccccc
	v_min_u32_dpp v202, v237, v237 quad_perm:[2,3,0,1] row_mask:0xf bank_mask:0xf
	v_max_u32_dpp v203, v237, v237 quad_perm:[2,3,0,1] row_mask:0xf bank_mask:0xf
	v_min_u32_dpp v204, v238, v238 quad_perm:[2,3,0,1] row_mask:0xf bank_mask:0xf
	v_max_u32_dpp v205, v238, v238 quad_perm:[2,3,0,1] row_mask:0xf bank_mask:0xf
	v_cndmask_b32_e64 v237, v203, v202, s[58:59]
	v_cndmask_b32_e64 v238, v205, v204, s[58:59]
	s_mov_b32 s58, 0x55555555
	s_mov_b32 s59, 0xaaaaaaaa
	v_min_u32_dpp v202, v237, v237 quad_perm:[1,0,3,2] row_mask:0xf bank_mask:0xf
	v_max_u32_dpp v203, v237, v237 quad_perm:[1,0,3,2] row_mask:0xf bank_mask:0xf
	v_min_u32_dpp v204, v238, v238 quad_perm:[1,0,3,2] row_mask:0xf bank_mask:0xf
	v_max_u32_dpp v205, v238, v238 quad_perm:[1,0,3,2] row_mask:0xf bank_mask:0xf
	v_cndmask_b32_e64 v237, v203, v202, s[58:59]
	v_cndmask_b32_e64 v238, v205, v204, s[58:59]
	s_nop 1
	v_permlane32_swap_b32_e32 v237, v238
	s_mov_b32 s58, 0xffff
	s_mov_b32 s59, 0xffff
	v_min_u32_e32 v202, v237, v238
	v_max_u32_e32 v203, v237, v238
	v_cndmask_b32_e64 v237, v203, v202, s[58:59]
	v_cndmask_b32_e64 v238, v202, v203, s[58:59]
	s_nop 1
	v_permlane32_swap_b32_e32 v237, v238
	s_mov_b32 s58, 0xffff
	s_mov_b32 s59, 0xffff
; __device__ __forceinline__ void expert_tokens(const unsigned char* __restrict__ UV, const float* __restrict__ US, const float* __restrict__ VS, ...
;     ...
;         const int ni0 = (int)nw0 & rmask, ni1 = (int)nw1 & rmask;
;         const float ng0 = __uint_as_float(nw0 & 0xFFFF0000u), ng1 = __uint_as_float(nw1 & 0xFFFF0000u);
;     ...
;             if (bi == 0) { nsu0 = US[ni0]; nsu1 = US[ni1]; nsv0 = VS[ni0]; nsv1 = VS[ni1]; }
	v_min_u32_e32 v202, v237, v238
	v_max_u32_e32 v203, v237, v238
	v_cndmask_b32_e64 v237, v203, v202, s[58:59]
	v_cndmask_b32_e64 v238, v202, v203, s[58:59]
	s_mov_b32 s58, 0xf0f00f0f
	s_mov_b32 s59, 0xf0f00f0f
	v_mov_b32_dpp v202, v237 row_half_mirror row_mask:0xf bank_mask:0xf
	v_mov_b32_dpp v204, v238 row_half_mirror row_mask:0xf bank_mask:0xf
	s_nop 0
	v_max_u32_dpp v203, v202, v237 quad_perm:[3,2,1,0] row_mask:0xf bank_mask:0xf
	v_max_u32_dpp v205, v204, v238 quad_perm:[3,2,1,0] row_mask:0xf bank_mask:0xf
	v_min_u32_dpp v202, v202, v237 quad_perm:[3,2,1,0] row_mask:0xf bank_mask:0xf
	v_min_u32_dpp v204, v204, v238 quad_perm:[3,2,1,0] row_mask:0xf bank_mask:0xf
	v_cndmask_b32_e64 v237, v203, v202, s[58:59]
	v_cndmask_b32_e64 v238, v205, v204, s[58:59]
	s_mov_b32 s58, 0xff0000ff
	s_mov_b32 s59, 0xff0000ff
	v_min_u32_dpp v202, v237, v237 row_ror:8 row_mask:0xf bank_mask:0xf
	v_max_u32_dpp v203, v237, v237 row_ror:8 row_mask:0xf bank_mask:0xf
	v_min_u32_dpp v204, v238, v238 row_ror:8 row_mask:0xf bank_mask:0xf
	v_max_u32_dpp v205, v238, v238 row_ror:8 row_mask:0xf bank_mask:0xf
	v_cndmask_b32_e64 v237, v203, v202, s[58:59]
	v_cndmask_b32_e64 v238, v205, v204, s[58:59]
	s_mov_b32 s58, 0xcccc3333
	s_mov_b32 s59, 0xcccc3333
	v_min_u32_dpp v202, v237, v237 quad_perm:[2,3,0,1] row_mask:0xf bank_mask:0xf
	v_max_u32_dpp v203, v237, v237 quad_perm:[2,3,0,1] row_mask:0xf bank_mask:0xf
	v_min_u32_dpp v204, v238, v238 quad_perm:[2,3,0,1] row_mask:0xf bank_mask:0xf
	v_max_u32_dpp v205, v238, v238 quad_perm:[2,3,0,1] row_mask:0xf bank_mask:0xf
	v_cndmask_b32_e64 v237, v203, v202, s[58:59]
	v_cndmask_b32_e64 v238, v205, v204, s[58:59]
	s_mov_b32 s58, 0xaaaa5555
	s_mov_b32 s59, 0xaaaa5555
	v_min_u32_dpp v202, v237, v237 quad_perm:[1,0,3,2] row_mask:0xf bank_mask:0xf
	v_max_u32_dpp v203, v237, v237 quad_perm:[1,0,3,2] row_mask:0xf bank_mask:0xf
	v_min_u32_dpp v204, v238, v238 quad_perm:[1,0,3,2] row_mask:0xf bank_mask:0xf
	v_max_u32_dpp v205, v238, v238 quad_perm:[1,0,3,2] row_mask:0xf bank_mask:0xf
	v_cndmask_b32_e64 v237, v203, v202, s[58:59]
	v_cndmask_b32_e64 v238, v205, v204, s[58:59]
	s_nop 1
	v_permlane16_swap_b32_e32 v237, v238
	v_min_u32_e32 v202, v237, v238
	v_max_u32_e32 v238, v237, v238
	v_mov_b32_e32 v237, v202
	s_nop 1
	v_permlane32_swap_b32_e32 v237, v238
	v_min_u32_e32 v202, v237, v238
	v_max_u32_e32 v238, v237, v238
	v_mov_b32_e32 v237, v202
	s_nop 1
	v_permlane16_swap_b32_e32 v237, v238
	v_min_u32_e32 v202, v237, v238
	v_max_u32_e32 v238, v237, v238
	v_mov_b32_e32 v237, v202
	s_mov_b32 s58, 0xf0f0f0f
	s_mov_b32 s59, 0xf0f0f0f
	v_mov_b32_dpp v202, v237 row_half_mirror row_mask:0xf bank_mask:0xf
	v_mov_b32_dpp v204, v238 row_half_mirror row_mask:0xf bank_mask:0xf
	s_nop 0
	v_max_u32_dpp v203, v202, v237 quad_perm:[3,2,1,0] row_mask:0xf bank_mask:0xf
	v_max_u32_dpp v205, v204, v238 quad_perm:[3,2,1,0] row_mask:0xf bank_mask:0xf
	v_min_u32_dpp v202, v202, v237 quad_perm:[3,2,1,0] row_mask:0xf bank_mask:0xf
	v_min_u32_dpp v204, v204, v238 quad_perm:[3,2,1,0] row_mask:0xf bank_mask:0xf
	v_cndmask_b32_e64 v237, v203, v202, s[58:59]
	v_cndmask_b32_e64 v238, v205, v204, s[58:59]
	s_mov_b32 s58, 0xff00ff
	s_mov_b32 s59, 0xff00ff
	v_min_u32_dpp v202, v237, v237 row_ror:8 row_mask:0xf bank_mask:0xf
	v_max_u32_dpp v203, v237, v237 row_ror:8 row_mask:0xf bank_mask:0xf
	v_min_u32_dpp v204, v238, v238 row_ror:8 row_mask:0xf bank_mask:0xf
	v_max_u32_dpp v205, v238, v238 row_ror:8 row_mask:0xf bank_mask:0xf
	v_cndmask_b32_e64 v237, v203, v202, s[58:59]
	v_cndmask_b32_e64 v238, v205, v204, s[58:59]
	s_mov_b32 s58, 0x33333333
	s_mov_b32 s59, 0x33333333
	v_min_u32_dpp v202, v237, v237 quad_perm:[2,3,0,1] row_mask:0xf bank_mask:0xf
	v_max_u32_dpp v203, v237, v237 quad_perm:[2,3,0,1] row_mask:0xf bank_mask:0xf
	v_min_u32_dpp v204, v238, v238 quad_perm:[2,3,0,1] row_mask:0xf bank_mask:0xf
	v_max_u32_dpp v205, v238, v238 quad_perm:[2,3,0,1] row_mask:0xf bank_mask:0xf
	v_cndmask_b32_e64 v237, v203, v202, s[58:59]
	v_cndmask_b32_e64 v238, v205, v204, s[58:59]
	s_mov_b32 s58, 0x55555555
	s_mov_b32 s59, 0x55555555
	v_min_u32_dpp v202, v237, v237 quad_perm:[1,0,3,2] row_mask:0xf bank_mask:0xf
	v_max_u32_dpp v203, v237, v237 quad_perm:[1,0,3,2] row_mask:0xf bank_mask:0xf
	v_min_u32_dpp v204, v238, v238 quad_perm:[1,0,3,2] row_mask:0xf bank_mask:0xf
	v_max_u32_dpp v205, v238, v238 quad_perm:[1,0,3,2] row_mask:0xf bank_mask:0xf
	v_cndmask_b32_e64 v237, v203, v202, s[58:59]
	v_cndmask_b32_e64 v238, v205, v204, s[58:59]
	s_nop 1
	v_permlane16_swap_b32_e32 v237, v238
	s_nop 1
	v_permlane32_swap_b32_e32 v237, v238
	v_xor_b32_e32 v237, s60, v237
	v_xor_b32_e32 v238, s60, v238
	v_alignbit_b32 v237, v237, v237, 16
	v_alignbit_b32 v238, v238, v238, 16
	v_and_b32_e32 v242, 0x3fff, v237
	v_and_b32_e32 v243, 0x3fff, v238
	v_lshlrev_b32_e32 v208, 2, v242
	v_lshlrev_b32_e32 v206, 2, v243
	global_load_dword v241, v208, s[12:13]
	global_load_dword v0, v206, s[12:13]
	global_load_dword v245, v208, s[14:15]
	global_load_dword v246, v206, s[14:15]
